# speedup vs baseline: 1.0014x; 1.0014x over previous
_Z11gemm_kernelILi1EEvPKDF16_S1_PKfPDF16_PfS5_S3_S3_S1_S3_:
	v_lshrrev_b32_e32 v4, 5, v0
	s_lshl_b32 s17, s2, 5
	v_or_b32_e32 v1, s17, v4
	s_load_dwordx4 s[8:11], s[0:1], 0x0
	s_load_dwordx2 s[12:13], s[0:1], 0x28
	v_or_b32_e32 v2, 8, v1
	v_min_i32_e32 v6, 0xc34f, v1
	v_min_i32_e32 v10, 0xc34f, v2
	v_ashrrev_i32_e32 v7, 31, v6
	v_ashrrev_i32_e32 v11, 31, v10
	v_mov_b32_e32 v3, 0
	v_and_b32_e32 v5, 31, v0
	v_lshlrev_b64 v[6:7], 9, v[6:7]
	v_lshlrev_b64 v[10:11], 9, v[10:11]
	s_waitcnt lgkmcnt(0)
	v_lshl_add_u64 v[6:7], s[8:9], 0, v[6:7]
	v_lshlrev_b32_e32 v8, 4, v5
	v_mov_b32_e32 v9, v3
	v_lshl_add_u64 v[10:11], s[8:9], 0, v[10:11]
	v_lshl_add_u64 v[6:7], v[6:7], 0, v[8:9]
	v_lshl_add_u64 v[10:11], v[10:11], 0, v[8:9]
	v_or_b32_e32 v2, 16, v1
	v_or_b32_e32 v1, 24, v1
	global_load_dwordx4 v[34:37], v[6:7], off nt
	global_load_dwordx4 v[38:41], v[10:11], off nt
	s_mov_b32 s22, 0x800000
	s_mov_b32 s23, 0
	v_lshl_add_u64 v[240:241], v[6:7], 0, s[22:23]
	v_lshl_add_u64 v[244:245], v[10:11], 0, s[22:23]
	global_load_dwordx4 v[240:243], v[240:241], off nt
	global_load_dwordx4 v[244:247], v[244:245], off nt
	v_min_i32_e32 v6, 0xc34f, v2
	v_min_i32_e32 v10, 0xc34f, v1
	v_ashrrev_i32_e32 v7, 31, v6
	v_ashrrev_i32_e32 v11, 31, v10
	v_lshlrev_b64 v[6:7], 9, v[6:7]
	v_lshlrev_b64 v[10:11], 9, v[10:11]
	v_lshl_add_u64 v[6:7], s[8:9], 0, v[6:7]
	v_lshl_add_u64 v[10:11], s[8:9], 0, v[10:11]
	v_lshlrev_b32_e32 v2, 9, v0
	v_lshl_add_u64 v[6:7], v[6:7], 0, v[8:9]
	v_lshl_add_u64 v[10:11], v[10:11], 0, v[8:9]
	v_and_b32_e32 v1, 63, v0
	v_and_b32_e32 v9, 0x18000, v2
	v_lshl_or_b32 v2, v1, 4, v9
	v_lshlrev_b32_e32 v1, 4, v0
	s_movk_i32 s3, 0x7c00
	global_load_dwordx4 v[58:61], v[6:7], off nt
	global_load_dwordx4 v[70:73], v[10:11], off nt
	v_lshl_add_u64 v[248:249], v[6:7], 0, s[22:23]
	v_lshl_add_u64 v[252:253], v[10:11], 0, s[22:23]
	global_load_dwordx4 v[248:251], v[248:249], off nt
	global_load_dwordx4 v[252:255], v[252:253], off nt
	v_lshl_add_u64 v[6:7], s[10:11], 0, v[2:3]
	v_or3_b32 v1, v1, v9, s3
	s_movk_i32 s3, 0x1000
	v_add_co_u32_e32 v10, vcc, s3, v6
	s_movk_i32 s3, 0x2000
	s_nop 0
	v_addc_co_u32_e32 v11, vcc, 0, v7, vcc
	v_add_co_u32_e32 v12, vcc, s3, v6
	s_movk_i32 s4, 0x3000
	s_nop 0
	v_addc_co_u32_e32 v13, vcc, 0, v7, vcc
	v_add_co_u32_e32 v14, vcc, s4, v6
	s_movk_i32 s4, 0x4000
	s_nop 0
	v_addc_co_u32_e32 v15, vcc, 0, v7, vcc
	v_add_co_u32_e32 v16, vcc, s4, v6
	s_movk_i32 s4, 0x5000
	s_nop 0
	v_addc_co_u32_e32 v17, vcc, 0, v7, vcc
	global_load_dwordx4 v[42:45], v[10:11], off offset:1024
	global_load_dwordx4 v[46:49], v[10:11], off offset:2048
	global_load_dwordx4 v[50:53], v[12:13], off offset:-4096
	global_load_dwordx4 v[54:57], v[12:13], off
	global_load_dwordx4 v[62:65], v[12:13], off offset:1024
	global_load_dwordx4 v[66:69], v[12:13], off offset:2048
	global_load_dwordx4 v[74:77], v[12:13], off offset:3072
	global_load_dwordx4 v[78:81], v[16:17], off offset:-4096
	global_load_dwordx4 v[82:85], v[10:11], off offset:3072
	global_load_dwordx4 v[86:89], v[14:15], off offset:1024
	global_load_dwordx4 v[90:93], v[14:15], off offset:2048
	global_load_dwordx4 v[94:97], v[14:15], off offset:3072
	global_load_dwordx4 v[98:101], v[16:17], off
	global_load_dwordx4 v[102:105], v[16:17], off offset:1024
	global_load_dwordx4 v[106:109], v2, s[10:11]
	global_load_dwordx4 v[110:113], v2, s[10:11] offset:1024
	global_load_dwordx4 v[114:117], v2, s[10:11] offset:2048
	global_load_dwordx4 v[118:121], v2, s[10:11] offset:3072
	global_load_dwordx4 v[122:125], v[16:17], off offset:2048
	global_load_dwordx4 v[126:129], v[16:17], off offset:3072
	v_add_co_u32_e32 v10, vcc, s4, v6
	s_movk_i32 s4, 0x6000
	s_nop 0
	v_addc_co_u32_e32 v11, vcc, 0, v7, vcc
	v_add_co_u32_e32 v12, vcc, s4, v6
	s_movk_i32 s4, 0x7000
	s_nop 0
	v_addc_co_u32_e32 v13, vcc, 0, v7, vcc
	v_add_co_u32_e32 v6, vcc, s4, v6
	global_load_dwordx4 v[130:133], v[12:13], off offset:-4096
	global_load_dwordx4 v[134:137], v[12:13], off
	global_load_dwordx4 v[138:141], v[10:11], off offset:1024
	global_load_dwordx4 v[142:145], v[10:11], off offset:2048
	global_load_dwordx4 v[146:149], v[10:11], off offset:3072
	v_addc_co_u32_e32 v7, vcc, 0, v7, vcc
	global_load_dwordx4 v[150:153], v[12:13], off offset:1024
	global_load_dwordx4 v[154:157], v[12:13], off offset:2048
	global_load_dwordx4 v[158:161], v[12:13], off offset:3072
	global_load_dwordx4 v[162:165], v[6:7], off
	global_load_dwordx4 v[166:169], v[6:7], off offset:1024
	global_load_dwordx4 v[170:173], v[6:7], off offset:2048
	global_load_dwordx4 v[174:177], v1, s[10:11]
	s_movk_i32 s10, 0x210
	v_mad_u32_u24 v213, v4, s10, v8
	s_mov_b32 s14, 0
	s_cmpk_gt_i32 s2, 0x61a
	v_bfe_u32 v1, v0, 4, 2
	v_and_b32_e32 v212, 15, v0
	s_waitcnt vmcnt(39)
	ds_write_b128 v213, v[34:37]
	s_waitcnt vmcnt(38)
	ds_write_b128 v213, v[38:41] offset:4224
	s_waitcnt vmcnt(35)
	ds_write_b128 v213, v[58:61] offset:8448
	s_waitcnt vmcnt(34)
	ds_write_b128 v213, v[70:73] offset:12672
	s_waitcnt vmcnt(17)
	s_waitcnt vmcnt(16)
	s_waitcnt vmcnt(15)
	s_waitcnt vmcnt(14)
	s_waitcnt vmcnt(13)
	s_waitcnt vmcnt(12)
	s_waitcnt vmcnt(11)
	s_waitcnt vmcnt(9)
	s_waitcnt vmcnt(8)
	s_waitcnt vmcnt(7)
	s_waitcnt vmcnt(6)
	s_waitcnt vmcnt(5)
	s_waitcnt vmcnt(4)
	s_waitcnt vmcnt(3)
	s_waitcnt vmcnt(2)
	s_waitcnt vmcnt(1)
	s_waitcnt vmcnt(0)
	v_mov_b64_e32 v[34:35], v[240:241]
	v_mov_b64_e32 v[36:37], v[242:243]
	v_mov_b64_e32 v[38:39], v[244:245]
	v_mov_b64_e32 v[40:41], v[246:247]
	v_mov_b64_e32 v[58:59], v[248:249]
	v_mov_b64_e32 v[60:61], v[250:251]
	v_mov_b64_e32 v[70:71], v[252:253]
	v_mov_b64_e32 v[72:73], v[254:255]
	s_waitcnt lgkmcnt(0)
	s_barrier
	s_cbranch_scc1 .LBB2_11
	s_load_dwordx2 s[4:5], s[0:1], 0x18
	s_load_dword s15, s[0:1], 0x50
	v_lshlrev_b32_e32 v2, 3, v5
	v_lshlrev_b32_e32 v2, 1, v2
	v_lshl_add_u64 v[210:211], s[8:9], 0, v[2:3]
	v_and_b32_e32 v2, 48, v0
	s_waitcnt lgkmcnt(0)
	s_add_i32 s0, s2, s15
	v_lshl_or_b32 v215, s0, 5, v4
	v_lshlrev_b32_e32 v4, 1, v0
	v_mad_u32_u24 v214, v212, s10, v2
	s_lshl_b32 s0, s2, 14
	v_lshlrev_b32_e32 v2, 9, v212
	v_and_b32_e32 v4, 0x180, v4
	v_mov_b32_e32 v16, v3
	v_mov_b32_e32 v17, v3
	v_or3_b32 v218, s0, v2, v4
	v_mov_b32_e32 v2, v3
	v_mov_b32_e32 v4, v3
	v_mov_b32_e32 v5, v3
	v_mov_b32_e32 v6, v3
	v_mov_b32_e32 v7, v3
	v_mov_b32_e32 v8, v3
	v_mov_b32_e32 v9, v3
	v_mov_b32_e32 v10, v3
	v_mov_b32_e32 v11, v3
	v_mov_b32_e32 v12, v3
	v_mov_b32_e32 v13, v3
	v_mov_b32_e32 v14, v3
	v_mov_b32_e32 v15, v3
	v_mov_b64_e32 v[32:33], v[16:17]
	s_mov_b32 s7, 0x20000
	s_mov_b32 s6, 0x186a000
	s_and_b32 s5, s5, 0xffff
	s_lshl_b32 s16, s15, 5
	v_add_u32_e32 v216, s17, v212
	v_lshlrev_b32_e32 v217, 4, v1
	s_lshl_b32 s17, s15, 14
	s_mov_b32 s18, 0xc350
	s_mov_b32 s19, s2
	s_mov_b32 s20, 0
	v_mov_b64_e32 v[30:31], v[14:15]
	v_mov_b64_e32 v[28:29], v[12:13]
	v_mov_b64_e32 v[26:27], v[10:11]
	v_mov_b64_e32 v[24:25], v[8:9]
	v_mov_b64_e32 v[22:23], v[6:7]
	v_mov_b64_e32 v[20:21], v[4:5]
	v_mov_b64_e32 v[18:19], v[2:3]
	s_add_i32 s19, s15, s19
	s_mov_b64 s[8:9], -1
	s_mov_b64 s[0:1], 0
	s_branch .LBB2_5

	.amdhsa_kernel _Z11gemm_kernelILi1EEvPKDF16_S1_PKfPDF16_PfS5_S3_S3_S1_S3_
		.amdhsa_group_segment_fixed_size 33792
		.amdhsa_private_segment_fixed_size 0
		.amdhsa_kernarg_size 336
		.amdhsa_user_sgpr_count 2
		.amdhsa_user_sgpr_dispatch_ptr 0
		.amdhsa_user_sgpr_queue_ptr 0
		.amdhsa_user_sgpr_kernarg_segment_ptr 1
		.amdhsa_user_sgpr_dispatch_id 0
		.amdhsa_user_sgpr_kernarg_preload_length 0
		.amdhsa_user_sgpr_kernarg_preload_offset 0
		.amdhsa_user_sgpr_private_segment_size 0
		.amdhsa_uses_dynamic_stack 0
		.amdhsa_enable_private_segment 0
		.amdhsa_system_sgpr_workgroup_id_x 1
		.amdhsa_system_sgpr_workgroup_id_y 0
		.amdhsa_system_sgpr_workgroup_id_z 0
		.amdhsa_system_sgpr_workgroup_info 0
		.amdhsa_system_vgpr_workitem_id 0
		.amdhsa_next_free_vgpr 256
		.amdhsa_next_free_sgpr 96
		.amdhsa_accum_offset 256
		.amdhsa_reserve_vcc 1
		.amdhsa_float_round_mode_32 0
		.amdhsa_float_round_mode_16_64 0
		.amdhsa_float_denorm_mode_32 3
		.amdhsa_float_denorm_mode_16_64 3
		.amdhsa_dx10_clamp 1
		.amdhsa_ieee_mode 1
		.amdhsa_fp16_overflow 0
		.amdhsa_tg_split 0
		.amdhsa_exception_fp_ieee_invalid_op 0
		.amdhsa_exception_fp_denorm_src 0
		.amdhsa_exception_fp_ieee_div_zero 0
		.amdhsa_exception_fp_ieee_overflow 0
		.amdhsa_exception_fp_ieee_underflow 0
		.amdhsa_exception_fp_ieee_inexact 0
		.amdhsa_exception_int_div_zero 0
	.end_amdhsa_kernel

amdhsa.kernels:
  - .agpr_count:     0
    .args:
      - .actual_access:  read_only
        .address_space:  global
        .offset:         0
        .size:           8
        .value_kind:     global_buffer
      - .actual_access:  read_only
        .address_space:  global
        .offset:         8
        .size:           8
        .value_kind:     global_buffer
      - .actual_access:  read_only
        .address_space:  global
        .offset:         16
        .size:           8
        .value_kind:     global_buffer
      - .actual_access:  read_only
        .address_space:  global
        .offset:         24
        .size:           8
        .value_kind:     global_buffer
      - .actual_access:  read_only
        .address_space:  global
        .offset:         32
        .size:           8
        .value_kind:     global_buffer
      - .address_space:  global
        .offset:         40
        .size:           8
        .value_kind:     global_buffer
      - .actual_access:  write_only
        .address_space:  global
        .offset:         48
        .size:           8
        .value_kind:     global_buffer
      - .actual_access:  write_only
        .address_space:  global
        .offset:         56
        .size:           8
        .value_kind:     global_buffer
      - .actual_access:  write_only
        .address_space:  global
        .offset:         64
        .size:           8
        .value_kind:     global_buffer
      - .actual_access:  write_only
        .address_space:  global
        .offset:         72
        .size:           8
        .value_kind:     global_buffer
      - .actual_access:  write_only
        .address_space:  global
        .offset:         80
        .size:           8
        .value_kind:     global_buffer
    .group_segment_fixed_size: 3132
    .kernarg_segment_align: 8
    .kernarg_segment_size: 88
    .language:       OpenCL C
    .language_version:
      - 2
      - 0
    .max_flat_workgroup_size: 256
    .name:           _Z11prep_kernelPKfPKiS0_S0_S0_PiP15HIP_vector_typeIjLj2EEP6OvfRecPDF16_S9_S9_
    .private_segment_fixed_size: 0
    .sgpr_count:     38
    .sgpr_spill_count: 0
    .symbol:         _Z11prep_kernelPKfPKiS0_S0_S0_PiP15HIP_vector_typeIjLj2EEP6OvfRecPDF16_S9_S9_.kd
    .uniform_work_group_size: 1
    .uses_dynamic_stack: false
    .vgpr_count:     42
    .vgpr_spill_count: 0
    .wavefront_size: 64
  - .agpr_count:     0
    .args:
      - .actual_access:  read_only
        .address_space:  global
        .offset:         0
        .size:           8
        .value_kind:     global_buffer
      - .actual_access:  read_only
        .address_space:  global
        .offset:         8
        .size:           8
        .value_kind:     global_buffer
      - .actual_access:  read_only
        .address_space:  global
        .offset:         16
        .size:           8
        .value_kind:     global_buffer
      - .address_space:  global
        .offset:         24
        .size:           8
        .value_kind:     global_buffer
      - .actual_access:  read_only
        .address_space:  global
        .offset:         32
        .size:           8
        .value_kind:     global_buffer
      - .actual_access:  write_only
        .address_space:  global
        .offset:         40
        .size:           8
        .value_kind:     global_buffer
    .group_segment_fixed_size: 12112
    .kernarg_segment_align: 8
    .kernarg_segment_size: 48
    .language:       OpenCL C
    .language_version:
      - 2
      - 0
    .max_flat_workgroup_size: 256
    .name:           _Z13gather_kernelPK15HIP_vector_typeIjLj2EEPKiPK6OvfRecPKDF16_PKfPDF16_
    .private_segment_fixed_size: 0
    .sgpr_count:     41
    .sgpr_spill_count: 0
    .symbol:         _Z13gather_kernelPK15HIP_vector_typeIjLj2EEPKiPK6OvfRecPKDF16_PKfPDF16_.kd
    .uniform_work_group_size: 1
    .uses_dynamic_stack: false
    .vgpr_count:     63
    .vgpr_spill_count: 0
    .wavefront_size: 64
  - .agpr_count:     0
    .args:
      - .actual_access:  read_only
        .address_space:  global
        .offset:         0
        .size:           8
        .value_kind:     global_buffer
      - .actual_access:  read_only
        .address_space:  global
        .offset:         8
        .size:           8
        .value_kind:     global_buffer
      - .actual_access:  read_only
        .address_space:  global
        .offset:         16
        .size:           8
        .value_kind:     global_buffer
      - .actual_access:  write_only
        .address_space:  global
        .offset:         24
        .size:           8
        .value_kind:     global_buffer
      - .actual_access:  read_only
        .address_space:  global
        .offset:         32
        .size:           8
        .value_kind:     global_buffer
      - .address_space:  global
        .offset:         40
        .size:           8
        .value_kind:     global_buffer
      - .actual_access:  read_only
        .address_space:  global
        .offset:         48
        .size:           8
        .value_kind:     global_buffer
      - .actual_access:  read_only
        .address_space:  global
        .offset:         56
        .size:           8
        .value_kind:     global_buffer
      - .actual_access:  read_only
        .address_space:  global
        .offset:         64
        .size:           8
        .value_kind:     global_buffer
      - .actual_access:  read_only
        .address_space:  global
        .offset:         72
        .size:           8
        .value_kind:     global_buffer
      - .offset:         80
        .size:           4
        .value_kind:     hidden_block_count_x
      - .offset:         84
        .size:           4
        .value_kind:     hidden_block_count_y
      - .offset:         88
        .size:           4
        .value_kind:     hidden_block_count_z
      - .offset:         92
        .size:           2
        .value_kind:     hidden_group_size_x
      - .offset:         94
        .size:           2
        .value_kind:     hidden_group_size_y
      - .offset:         96
        .size:           2
        .value_kind:     hidden_group_size_z
      - .offset:         98
        .size:           2
        .value_kind:     hidden_remainder_x
      - .offset:         100
        .size:           2
        .value_kind:     hidden_remainder_y
      - .offset:         102
        .size:           2
        .value_kind:     hidden_remainder_z
      - .offset:         120
        .size:           8
        .value_kind:     hidden_global_offset_x
      - .offset:         128
        .size:           8
        .value_kind:     hidden_global_offset_y
      - .offset:         136
        .size:           8
        .value_kind:     hidden_global_offset_z
      - .offset:         144
        .size:           2
        .value_kind:     hidden_grid_dims
    .group_segment_fixed_size: 33792
    .kernarg_segment_align: 8
    .kernarg_segment_size: 336
    .language:       OpenCL C
    .language_version:
      - 2
      - 0
    .max_flat_workgroup_size: 256
    .name:           _Z11gemm_kernelILi1EEvPKDF16_S1_PKfPDF16_PfS5_S3_S3_S1_S3_
    .private_segment_fixed_size: 0
    .sgpr_count:     27
    .sgpr_spill_count: 0
    .symbol:         _Z11gemm_kernelILi1EEvPKDF16_S1_PKfPDF16_PfS5_S3_S3_S1_S3_.kd
    .uniform_work_group_size: 1
    .uses_dynamic_stack: false
    .vgpr_count:     256
    .vgpr_spill_count: 0
    .wavefront_size: 64
  - .agpr_count:     0
    .args:
      - .actual_access:  read_only
        .address_space:  global
        .offset:         0
        .size:           8
        .value_kind:     global_buffer
      - .actual_access:  read_only
        .address_space:  global
        .offset:         8
        .size:           8
        .value_kind:     global_buffer
      - .actual_access:  read_only
        .address_space:  global
        .offset:         16
        .size:           8
        .value_kind:     global_buffer
      - .actual_access:  read_only
        .address_space:  global
        .offset:         24
        .size:           8
        .value_kind:     global_buffer
      - .actual_access:  write_only
        .address_space:  global
        .offset:         32
        .size:           8
        .value_kind:     global_buffer
      - .actual_access:  read_only
        .address_space:  global
        .offset:         40
        .size:           8
        .value_kind:     global_buffer
      - .actual_access:  read_only
        .address_space:  global
        .offset:         48
        .size:           8
        .value_kind:     global_buffer
      - .actual_access:  read_only
        .address_space:  global
        .offset:         56
        .size:           8
        .value_kind:     global_buffer
      - .actual_access:  read_only
        .address_space:  global
        .offset:         64
        .size:           8
        .value_kind:     global_buffer
      - .actual_access:  read_only
        .address_space:  global
        .offset:         72
        .size:           8
        .value_kind:     global_buffer
      - .offset:         80
        .size:           4
        .value_kind:     hidden_block_count_x
      - .offset:         84
        .size:           4
        .value_kind:     hidden_block_count_y
      - .offset:         88
        .size:           4
        .value_kind:     hidden_block_count_z
      - .offset:         92
        .size:           2
        .value_kind:     hidden_group_size_x
      - .offset:         94
        .size:           2
        .value_kind:     hidden_group_size_y
      - .offset:         96
        .size:           2
        .value_kind:     hidden_group_size_z
      - .offset:         98
        .size:           2
        .value_kind:     hidden_remainder_x
      - .offset:         100
        .size:           2
        .value_kind:     hidden_remainder_y
      - .offset:         102
        .size:           2
        .value_kind:     hidden_remainder_z
      - .offset:         120
        .size:           8
        .value_kind:     hidden_global_offset_x
      - .offset:         128
        .size:           8
        .value_kind:     hidden_global_offset_y
      - .offset:         136
        .size:           8
        .value_kind:     hidden_global_offset_z
      - .offset:         144
        .size:           2
        .value_kind:     hidden_grid_dims
    .group_segment_fixed_size: 33792
    .kernarg_segment_align: 8
    .kernarg_segment_size: 336
    .language:       OpenCL C
    .language_version:
      - 2
      - 0
    .max_flat_workgroup_size: 256
    .name:           _Z11gemm_kernelILi2EEvPKDF16_S1_PKfPDF16_PfS5_S3_S3_S1_S3_
    .private_segment_fixed_size: 0
    .sgpr_count:     23
    .sgpr_spill_count: 0
    .symbol:         _Z11gemm_kernelILi2EEvPKDF16_S1_PKfPDF16_PfS5_S3_S3_S1_S3_.kd
    .uniform_work_group_size: 1
    .uses_dynamic_stack: false
    .vgpr_count:     256
    .vgpr_spill_count: 0
    .wavefront_size: 64
